# SSD: causal-mask flags computed once per task instead of per element per step
# speedup vs baseline: 1.0674x; 1.0002x over previous
.LBB0_739:
	s_or_b64 exec, exec, s[10:11]
	s_mul_i32 s11, s38, 0xa0000
	s_mul_hi_i32 s10, s38, 0xa0000
	s_add_u32 s11, s24, s11
	s_addc_u32 s37, s25, s10
	s_lshl_b32 s10, s40, 1
	s_add_u32 s10, s11, s10
	s_addc_u32 s11, s37, 0
	s_lshl_b32 s37, s28, 4
	v_ashrrev_i32_e32 v7, 3, v98
	s_and_b32 s37, s37, 0x80
	v_add_u32_e32 v2, s37, v7
	v_add_u32_e32 v102, 0x400, v2
	v_ashrrev_i32_e32 v103, 31, v102
	v_lshlrev_b32_e32 v4, 3, v98
	v_lshlrev_b64 v[2:3], 9, v[102:103]
	v_and_b32_e32 v8, 56, v4
	v_lshl_add_u64 v[2:3], s[10:11], 0, v[2:3]
	v_lshlrev_b32_e32 v4, 1, v8
	v_mov_b32_e32 v5, v99
	v_lshl_add_u64 v[2:3], v[2:3], 0, v[4:5]
	v_add_co_u32_e32 v10, vcc, s67, v2
	s_lshl_b32 s41, s75, 4
	s_nop 0
	v_addc_co_u32_e32 v11, vcc, 0, v3, vcc
	global_load_dwordx4 v[38:41], v[2:3], off
	global_load_dwordx4 v[42:45], v[10:11], off
	v_add_co_u32_e32 v10, vcc, s68, v2
	s_lshl_b32 s40, s28, 6
	s_and_b32 s54, s41, 32
	v_addc_co_u32_e32 v11, vcc, 0, v3, vcc
	s_or_b32 s40, s40, s54
	v_add_co_u32_e32 v2, vcc, s69, v2
	v_add_u32_e32 v104, s40, v7
	s_nop 0
	v_addc_co_u32_e32 v3, vcc, 0, v3, vcc
	v_ashrrev_i32_e32 v105, 31, v104
	global_load_dwordx4 v[46:49], v[10:11], off
	global_load_dwordx4 v[50:53], v[2:3], off
	v_lshlrev_b64 v[2:3], 9, v[104:105]
	v_lshl_add_u64 v[2:3], s[10:11], 0, v[2:3]
	v_lshl_add_u64 v[2:3], v[2:3], 0, v[4:5]
	global_load_dwordx4 v[54:57], v[2:3], off
	s_lshl_b64 s[42:43], s[38:39], 11
	s_and_b64 s[52:53], s[6:7], exec
	v_and_b32_e32 v3, 63, v98
	s_cselect_b32 s76, s63, s47
	s_cselect_b32 s77, s62, s46
	s_lshl_b32 s37, s37, 1
	v_ashrrev_i32_e32 v2, 4, v98
	v_lshlrev_b32_e32 v4, 2, v3
	s_add_u32 s52, s16, s37
	v_or_b32_e32 v127, 0x12000, v4
	v_or_b32_e32 v128, 0x12100, v4
	v_or_b32_e32 v129, 0x12200, v4
	v_or_b32_e32 v130, 0x12300, v4
	v_xor_b32_e32 v4, v2, v98
	s_addc_u32 s53, s17, 0
	s_lshl_b32 s28, s28, 7
	v_cmp_eq_u32_e64 s[10:11], 0, v3
	v_lshlrev_b32_e32 v3, 8, v2
	v_lshlrev_b32_e32 v4, 4, v4
	s_add_u32 s28, s50, s28
	v_and_or_b32 v131, v4, s70, v3
	v_xor_b32_e32 v4, v7, v98
	s_addc_u32 s37, s51, 0
	s_lshl_b32 s50, s54, 1
	v_and_b32_e32 v125, 15, v98
	v_lshlrev_b32_e32 v3, 7, v7
	v_lshlrev_b32_e32 v4, 4, v4
	s_add_u32 s50, s28, s50
	v_and_or_b32 v132, v4, s71, v3
	v_lshlrev_b32_e32 v4, 4, v125
	s_addc_u32 s51, s37, 0
	v_lshl_add_u64 v[106:107], s[52:53], 0, v[4:5]
	v_and_b32_e32 v4, 0xffffffc0, v98
	s_and_b64 s[52:53], s[6:7], exec
	v_ashrrev_i32_e32 v3, 31, v2
	v_add_u32_e32 v134, 0x12000, v4
	v_add_u32_e32 v138, 0x12300, v4
	s_cselect_b32 s28, s72, 0x1d8
	v_mov_b32_e32 v4, v99
	v_ashrrev_i32_e32 v9, 6, v98
	s_add_u32 s78, s26, s28
	v_lshl_add_u64 v[108:109], s[42:43], 0, v[2:3]
	v_mov_b32_e32 v2, v99
	v_mov_b32_e32 v3, v99
	v_mov_b64_e32 v[16:17], v[4:5]
	v_mov_b64_e32 v[24:25], v[4:5]
	v_mov_b64_e32 v[32:33], v[4:5]
	v_mov_b64_e32 v[12:13], v[4:5]
	v_mov_b64_e32 v[20:21], v[4:5]
	v_mov_b64_e32 v[28:29], v[4:5]
	v_mov_b64_e32 v[36:37], v[4:5]
	s_mul_hi_i32 s41, s38, 0x500
	s_mul_i32 s40, s38, 0x500
	v_bfe_u32 v126, v98, 4, 2
	v_lshlrev_b32_e32 v133, 12, v9
	v_lshlrev_b32_e32 v136, 4, v9
	v_lshlrev_b32_e32 v137, 11, v9
	v_lshlrev_b32_e32 v139, 5, v9
	s_addc_u32 s79, s27, 0
	s_mov_b32 s80, -4
	v_lshlrev_b32_e32 v98, 1, v8
	v_mov_b64_e32 v[14:15], v[2:3]
	v_mov_b64_e32 v[22:23], v[2:3]
	v_mov_b64_e32 v[30:31], v[2:3]
	v_mov_b64_e32 v[10:11], v[2:3]
	v_mov_b64_e32 v[18:19], v[2:3]
	v_mov_b64_e32 v[26:27], v[2:3]
	v_mov_b64_e32 v[34:35], v[2:3]
	v_mov_b32_e32 v7, v6
	v_mov_b32_e32 v8, v6
	v_mov_b32_e32 v9, v6
	v_mov_b32_e32 v58, v6
	v_mov_b32_e32 v59, v6
	v_mov_b32_e32 v60, v6
	v_mov_b32_e32 v61, v6
	v_mov_b32_e32 v66, v6
	v_mov_b32_e32 v67, v6
	v_mov_b32_e32 v68, v6
	v_mov_b32_e32 v69, v6
	v_mov_b32_e32 v62, v6
	v_mov_b32_e32 v63, v6
	v_mov_b32_e32 v64, v6
	v_mov_b32_e32 v65, v6
	v_and_b32_e32 v216, 15, v0
	v_lshrrev_b32_e32 v217, 6, v0
	v_lshlrev_b32_e32 v217, 4, v217
	v_bfe_u32 v218, v0, 4, 2
	v_lshl_add_u32 v217, v218, 2, v217
	v_sub_u32_e32 v216, v216, v217
	s_and_b64 vcc, exec, s[6:7]
	s_cbranch_vccz .Lmy_fdir1
	v_cmp_ge_i32_e32 vcc, 0, v216
	s_nop 1
	v_cndmask_b32_e64 v200, 0, 1, vcc
	v_cmp_ge_i32_e32 vcc, 1, v216
	s_nop 1
	v_cndmask_b32_e64 v201, 0, 1, vcc
	v_cmp_ge_i32_e32 vcc, 2, v216
	s_nop 1
	v_cndmask_b32_e64 v202, 0, 1, vcc
	v_cmp_ge_i32_e32 vcc, 3, v216
	s_nop 1
	v_cndmask_b32_e64 v203, 0, 1, vcc
	v_cmp_ge_i32_e32 vcc, -16, v216
	s_nop 1
	v_cndmask_b32_e64 v204, 0, 1, vcc
	v_cmp_ge_i32_e32 vcc, -15, v216
	s_nop 1
	v_cndmask_b32_e64 v205, 0, 1, vcc
	v_cmp_ge_i32_e32 vcc, -14, v216
	s_nop 1
	v_cndmask_b32_e64 v206, 0, 1, vcc
	v_cmp_ge_i32_e32 vcc, -13, v216
	s_nop 1
	v_cndmask_b32_e64 v207, 0, 1, vcc
	v_cmp_ge_i32_e32 vcc, -32, v216
	s_nop 1
	v_cndmask_b32_e64 v208, 0, 1, vcc
	v_cmp_ge_i32_e32 vcc, -31, v216
	s_nop 1
	v_cndmask_b32_e64 v209, 0, 1, vcc
	v_cmp_ge_i32_e32 vcc, -30, v216
	s_nop 1
	v_cndmask_b32_e64 v210, 0, 1, vcc
	v_cmp_ge_i32_e32 vcc, -29, v216
	s_nop 1
	v_cndmask_b32_e64 v211, 0, 1, vcc
	v_cmp_ge_i32_e32 vcc, -48, v216
	s_nop 1
	v_cndmask_b32_e64 v212, 0, 1, vcc
	v_cmp_ge_i32_e32 vcc, -47, v216
	s_nop 1
	v_cndmask_b32_e64 v213, 0, 1, vcc
	v_cmp_ge_i32_e32 vcc, -46, v216
	s_nop 1
	v_cndmask_b32_e64 v214, 0, 1, vcc
	v_cmp_ge_i32_e32 vcc, -45, v216
	s_nop 1
	v_cndmask_b32_e64 v215, 0, 1, vcc
	s_branch .Lmy_fdone
.Lmy_fdir1:
	v_cmp_le_i32_e32 vcc, 0, v216
	s_nop 1
	v_cndmask_b32_e64 v200, 0, 1, vcc
	v_cmp_le_i32_e32 vcc, 1, v216
	s_nop 1
	v_cndmask_b32_e64 v201, 0, 1, vcc
	v_cmp_le_i32_e32 vcc, 2, v216
	s_nop 1
	v_cndmask_b32_e64 v202, 0, 1, vcc
	v_cmp_le_i32_e32 vcc, 3, v216
	s_nop 1
	v_cndmask_b32_e64 v203, 0, 1, vcc
	v_cmp_le_i32_e32 vcc, -16, v216
	s_nop 1
	v_cndmask_b32_e64 v204, 0, 1, vcc
	v_cmp_le_i32_e32 vcc, -15, v216
	s_nop 1
	v_cndmask_b32_e64 v205, 0, 1, vcc
	v_cmp_le_i32_e32 vcc, -14, v216
	s_nop 1
	v_cndmask_b32_e64 v206, 0, 1, vcc
	v_cmp_le_i32_e32 vcc, -13, v216
	s_nop 1
	v_cndmask_b32_e64 v207, 0, 1, vcc
	v_cmp_le_i32_e32 vcc, -32, v216
	s_nop 1
	v_cndmask_b32_e64 v208, 0, 1, vcc
	v_cmp_le_i32_e32 vcc, -31, v216
	s_nop 1
	v_cndmask_b32_e64 v209, 0, 1, vcc
	v_cmp_le_i32_e32 vcc, -30, v216
	s_nop 1
	v_cndmask_b32_e64 v210, 0, 1, vcc
	v_cmp_le_i32_e32 vcc, -29, v216
	s_nop 1
	v_cndmask_b32_e64 v211, 0, 1, vcc
	v_cmp_le_i32_e32 vcc, -48, v216
	s_nop 1
	v_cndmask_b32_e64 v212, 0, 1, vcc
	v_cmp_le_i32_e32 vcc, -47, v216
	s_nop 1
	v_cndmask_b32_e64 v213, 0, 1, vcc
	v_cmp_le_i32_e32 vcc, -46, v216
	s_nop 1
	v_cndmask_b32_e64 v214, 0, 1, vcc
	v_cmp_le_i32_e32 vcc, -45, v216
	s_nop 1
	v_cndmask_b32_e64 v215, 0, 1, vcc
.Lmy_fdone:
	s_branch .LBB0_741

.LBB0_756:
	s_waitcnt lgkmcnt(0)
	s_barrier
	ds_read_b32 v143, v120
	v_add_u32_e32 v74, 4, v140
	v_lshlrev_b32_e32 v89, 1, v110
	v_bitop3_b32 v111, v110, v140, 7 bitop3:0x6c
	s_mov_b64 s[54:55], -1
	s_and_b64 vcc, exec, s[52:53]
	v_lshlrev_b32_e32 v145, 2, v140
	v_and_b32_e32 v146, 14, v89
	v_lshlrev_b32_e32 v144, 7, v110
	v_lshlrev_b32_e32 v147, 4, v111
	v_bitop3_b32 v148, v74, v110, 7 bitop3:0x78
	s_cbranch_vccz .LBB0_758
	v_lshlrev_b32_e32 v86, 8, v110
	v_bitop3_b32 v70, v110, v140, 15 bitop3:0x6c
	v_add_u32_e32 v87, v133, v86
	v_lshlrev_b32_e32 v75, 4, v70
	v_add_u32_e32 v70, v87, v75
	ds_read_b128 v[70:73], v70
	v_bitop3_b32 v74, v74, v110, 15 bitop3:0x78
	v_lshlrev_b32_e32 v88, 4, v74
	v_add_u32_e32 v149, v86, v75
	v_add_u32_e32 v74, v87, v88
	ds_read_b128 v[78:81], v149 offset:16384
	ds_read_b128 v[74:77], v74
	ds_read_b128 v[82:85], v149 offset:20480
	v_add_u32_e32 v116, 8, v140
	v_add_u32_e32 v174, v86, v88
	ds_read_b128 v[90:93], v149 offset:24576
	ds_read_b128 v[94:97], v149 offset:28672
	ds_read_b128 v[112:115], v174 offset:16384
	v_bitop3_b32 v88, v116, v110, 15 bitop3:0x78
	ds_read_b128 v[116:119], v174 offset:20480
	s_waitcnt lgkmcnt(6)
	v_mfma_f32_16x16x32_bf16 v[78:81], v[70:73], v[78:81], 0
	v_lshlrev_b32_e32 v88, 4, v88
	v_add_u32_e32 v175, v86, v88
	v_lshlrev_b32_e32 v142, 2, v140
	s_waitcnt lgkmcnt(4)
	v_mfma_f32_16x16x32_bf16 v[82:85], v[70:73], v[82:85], 0
	s_lshl_b32 s28, s81, 6
	s_ashr_i32 s37, s28, 31
	s_add_u32 s52, s42, s28
	s_waitcnt lgkmcnt(1)
	v_mfma_f32_16x16x32_bf16 v[112:115], v[74:77], v[112:115], v[78:81]
	s_addc_u32 s53, s43, s37
	s_mov_b64 s[54:55], 0
	s_nop 0
	v_add_u32_e32 v78, v87, v88
	s_waitcnt lgkmcnt(0)
	v_mfma_f32_16x16x32_bf16 v[116:119], v[74:77], v[116:119], v[82:85]
	ds_read_b128 v[78:81], v78
	ds_read_b128 v[154:157], v174 offset:24576
	s_nop 0
	v_add_u32_e32 v82, 12, v140
	v_bitop3_b32 v141, v82, v110, 15 bitop3:0x78
	ds_read_b128 v[82:85], v174 offset:28672
	v_mfma_f32_16x16x32_bf16 v[90:93], v[70:73], v[90:93], 0
	v_lshlrev_b32_e32 v141, 4, v141
	v_add_u32_e32 v176, v86, v141
	v_mfma_f32_16x16x32_bf16 v[94:97], v[70:73], v[94:97], 0
	s_waitcnt lgkmcnt(1)
	v_mfma_f32_16x16x32_bf16 v[90:93], v[74:77], v[154:157], v[90:93]
	ds_read_b128 v[154:157], v175 offset:16384
	s_waitcnt lgkmcnt(1)
	v_mfma_f32_16x16x32_bf16 v[94:97], v[74:77], v[82:85], v[94:97]
	v_add_u32_e32 v82, v87, v141
	ds_read_b128 v[82:85], v82
	ds_read_b128 v[158:161], v175 offset:20480
	v_and_b32_e32 v141, 14, v89
	s_waitcnt lgkmcnt(2)
	v_mfma_f32_16x16x32_bf16 v[112:115], v[78:81], v[154:157], v[112:115]
	s_waitcnt lgkmcnt(0)
	v_mfma_f32_16x16x32_bf16 v[116:119], v[78:81], v[158:161], v[116:119]
	ds_read_b128 v[154:157], v175 offset:24576
	ds_read_b128 v[158:161], v175 offset:28672
	s_waitcnt lgkmcnt(1)
	v_mfma_f32_16x16x32_bf16 v[154:157], v[78:81], v[154:157], v[90:93]
	s_waitcnt lgkmcnt(0)
	v_mfma_f32_16x16x32_bf16 v[158:161], v[78:81], v[158:161], v[94:97]
	s_nop 0
	ds_read_b128 v[90:93], v176 offset:16384
	s_nop 0
	ds_read_b128 v[94:97], v176 offset:20480
	s_waitcnt lgkmcnt(1)
	v_mfma_f32_16x16x32_bf16 v[162:165], v[82:85], v[90:93], v[112:115]
	s_nop 2
	ds_read_b128 v[112:115], v176 offset:24576
	ds_read_b128 v[166:169], v176 offset:28672
	s_waitcnt lgkmcnt(0)
	s_barrier
	s_waitcnt lgkmcnt(2)
	v_mfma_f32_16x16x32_bf16 v[170:173], v[82:85], v[94:97], v[116:119]
	s_nop 2
	v_lshlrev_b32_e32 v117, 4, v140
	s_waitcnt lgkmcnt(1)
	v_mfma_f32_16x16x32_bf16 v[94:97], v[82:85], v[112:115], v[154:157]
	v_lshlrev_b32_e32 v113, 2, v110
	v_add_u32_e32 v86, v134, v117
	v_add_u32_e32 v115, 0x12000, v113
	ds_read_b128 v[90:93], v86
	ds_read2_b32 v[154:155], v115 offset1:16
	v_add_u32_e32 v113, 0x12100, v113
	v_add_u32_e32 v112, v142, v136
	ds_read2_b32 v[156:157], v113 offset1:16
	s_waitcnt lgkmcnt(1)
	v_sub_f32_e32 v116, v90, v154
	v_mul_f32_e32 v116, 0x3fb8aa3b, v116
	v_exp_f32_e32 v116, v116
	v_lshrrev_b32_e32 v119, 3, v110
	v_mul_f32_e32 v116, v162, v116
	s_waitcnt lgkmcnt(0)
	v_mul_f32_e32 v116, v156, v116
	v_cvt_pk_bf16_f32 v116, v116, s0
	v_cmp_ne_u32_e32 vcc, 0, v200
	v_mfma_f32_16x16x32_bf16 v[86:89], v[82:85], v[166:169], v[158:161]
	v_sub_f32_e32 v118, v91, v154
	v_cndmask_b32_e32 v114, 0, v116, vcc
	v_bitop3_b32 v116, v142, v119, 4 bitop3:0x6c
	v_lshlrev_b32_e32 v158, 7, v112
	v_lshl_add_u32 v116, v116, 4, v158
	v_mul_f32_e32 v118, 0x3fb8aa3b, v118
	v_or_b32_e32 v116, v116, v141
	v_exp_f32_e32 v118, v118
	ds_write_b16 v116, v114 offset:16384
	v_or_b32_e32 v114, 1, v112
	v_mul_f32_e32 v118, v163, v118
	v_mul_f32_e32 v118, v156, v118
	v_cvt_pk_bf16_f32 v118, v118, s0
	v_sub_f32_e32 v160, v92, v154
	v_cmp_ne_u32_e32 vcc, 0, v201
	v_lshlrev_b32_e32 v159, 7, v114
	v_mul_f32_e32 v160, 0x3fb8aa3b, v160
	v_cndmask_b32_e32 v116, 0, v118, vcc
	v_bitop3_b32 v118, v114, v119, 5 bitop3:0x6c
	v_lshl_add_u32 v118, v118, 4, v159
	v_or_b32_e32 v118, v118, v141
	ds_write_b16 v118, v116 offset:16384
	v_or_b32_e32 v116, 2, v112
	v_exp_f32_e32 v160, v160
	v_sub_f32_e32 v154, v93, v154
	v_mul_f32_e32 v154, 0x3fb8aa3b, v154
	v_mul_f32_e32 v160, v164, v160
	v_mul_f32_e32 v160, v156, v160
	v_cvt_pk_bf16_f32 v160, v160, s0
	v_cmp_ne_u32_e32 vcc, 0, v202
	v_bitop3_b32 v161, v116, v119, 6 bitop3:0x6c
	v_exp_f32_e32 v154, v154
	v_cndmask_b32_e32 v118, 0, v160, vcc
	v_lshlrev_b32_e32 v160, 7, v116
	v_lshl_add_u32 v161, v161, 4, v160
	v_or_b32_e32 v161, v161, v141
	ds_write_b16 v161, v118 offset:16384
	v_or_b32_e32 v118, 3, v112
	v_mul_f32_e32 v154, v165, v154
	v_mul_f32_e32 v154, v156, v154
	v_bitop3_b32 v119, v118, v119, 7 bitop3:0x6c
	v_cvt_pk_bf16_f32 v154, v154, s0
	v_cmp_ne_u32_e32 vcc, 0, v203
	v_lshlrev_b32_e32 v161, 7, v118
	v_lshl_add_u32 v119, v119, 4, v161
	v_sub_f32_e32 v162, v90, v155
	v_cndmask_b32_e32 v154, 0, v154, vcc
	v_or_b32_e32 v119, v119, v141
	v_mul_f32_e32 v162, 0x3fb8aa3b, v162
	ds_write_b16 v119, v154 offset:16384
	v_add_u32_e32 v119, 16, v110
	v_exp_f32_e32 v162, v162
	v_lshrrev_b32_e32 v154, 3, v119
	v_mul_f32_e32 v162, v170, v162
	v_mul_f32_e32 v162, v157, v162
	v_cvt_pk_bf16_f32 v162, v162, s0
	v_cmp_ne_u32_e32 vcc, 0, v204
	s_nop 1
	s_nop 0
	v_cndmask_b32_e32 v156, 0, v162, vcc
	v_bitop3_b32 v162, v142, v154, 4 bitop3:0x6c
	v_lshl_add_u32 v162, v162, 4, v158
	v_or_b32_e32 v162, v162, v141
	ds_write_b16 v162, v156 offset:16384
	v_sub_f32_e32 v162, v91, v155
	v_mul_f32_e32 v162, 0x3fb8aa3b, v162
	v_exp_f32_e32 v162, v162
	s_nop 0
	v_mul_f32_e32 v162, v171, v162
	s_nop 0
	v_mul_f32_e32 v162, v157, v162
	v_cvt_pk_bf16_f32 v162, v162, s0
	v_cmp_ne_u32_e32 vcc, 0, v205
	s_nop 1
	s_nop 0
	v_cndmask_b32_e32 v156, 0, v162, vcc
	v_bitop3_b32 v162, v114, v154, 5 bitop3:0x6c
	v_lshl_add_u32 v162, v162, 4, v159
	v_or_b32_e32 v162, v162, v141
	ds_write_b16 v162, v156 offset:16384
	v_sub_f32_e32 v162, v92, v155
	v_mul_f32_e32 v162, 0x3fb8aa3b, v162
	v_exp_f32_e32 v162, v162
	v_sub_f32_e32 v155, v93, v155
	v_mul_f32_e32 v155, 0x3fb8aa3b, v155
	v_mul_f32_e32 v162, v172, v162
	v_mul_f32_e32 v162, v157, v162
	v_cvt_pk_bf16_f32 v162, v162, s0
	v_cmp_ne_u32_e32 vcc, 0, v206
	v_exp_f32_e32 v155, v155
	s_nop 0
	v_cndmask_b32_e32 v156, 0, v162, vcc
	v_bitop3_b32 v162, v116, v154, 6 bitop3:0x6c
	v_lshl_add_u32 v162, v162, 4, v160
	v_or_b32_e32 v162, v162, v141
	ds_write_b16 v162, v156 offset:16384
	v_mul_f32_e32 v155, v173, v155
	v_mul_f32_e32 v155, v157, v155
	v_bitop3_b32 v154, v118, v154, 7 bitop3:0x6c
	v_cvt_pk_bf16_f32 v155, v155, s0
	v_cmp_ne_u32_e32 vcc, 0, v207
	v_lshl_add_u32 v154, v154, 4, v161
	v_or_b32_e32 v154, v154, v141
	v_cndmask_b32_e32 v119, 0, v155, vcc
	ds_write_b16 v154, v119 offset:16384
	ds_read2_b32 v[154:155], v115 offset0:32 offset1:48
	ds_read2_b32 v[156:157], v113 offset0:32 offset1:48
	v_add_u32_e32 v119, 32, v110
	v_lshrrev_b32_e32 v113, 3, v119
	s_waitcnt lgkmcnt(1)
	v_sub_f32_e32 v162, v90, v154
	v_mul_f32_e32 v162, 0x3fb8aa3b, v162
	v_exp_f32_e32 v162, v162
	v_sub_f32_e32 v90, v90, v155
	v_mul_f32_e32 v94, v94, v162
	s_waitcnt lgkmcnt(0)
	v_mul_f32_e32 v94, v156, v94
	v_cmp_ne_u32_e32 vcc, 0, v208
	v_bitop3_b32 v115, v142, v113, 4 bitop3:0x6c
	v_cvt_pk_bf16_f32 v94, v94, s0
	v_lshl_add_u32 v115, v115, 4, v158
	v_cndmask_b32_e32 v94, 0, v94, vcc
	v_or_b32_e32 v115, v115, v141
	ds_write_b16 v115, v94 offset:16384
	v_sub_f32_e32 v115, v91, v154
	v_mul_f32_e32 v115, 0x3fb8aa3b, v115
	v_exp_f32_e32 v115, v115
	v_mul_f32_e32 v90, 0x3fb8aa3b, v90
	v_exp_f32_e32 v90, v90
	v_mul_f32_e32 v95, v95, v115
	v_mul_f32_e32 v95, v156, v95
	v_cvt_pk_bf16_f32 v95, v95, s0
	v_cmp_ne_u32_e32 vcc, 0, v209
	v_mul_f32_e32 v86, v86, v90
	v_mul_f32_e32 v86, v157, v86
	v_cndmask_b32_e32 v94, 0, v95, vcc
	v_bitop3_b32 v95, v114, v113, 5 bitop3:0x6c
	v_lshl_add_u32 v95, v95, 4, v159
	v_or_b32_e32 v95, v95, v141
	ds_write_b16 v95, v94 offset:16384
	v_sub_f32_e32 v95, v92, v154
	v_mul_f32_e32 v95, 0x3fb8aa3b, v95
	v_exp_f32_e32 v95, v95
	v_cvt_pk_bf16_f32 v86, v86, s0
	v_mul_f32_e32 v95, v96, v95
	v_mul_f32_e32 v95, v156, v95
	v_cvt_pk_bf16_f32 v95, v95, s0
	v_cmp_ne_u32_e32 vcc, 0, v210
	v_ashrrev_i32_e32 v115, 31, v114
	s_nop 0
	v_cndmask_b32_e32 v94, 0, v95, vcc
	v_bitop3_b32 v95, v116, v113, 6 bitop3:0x6c
	v_lshl_add_u32 v95, v95, 4, v160
	v_or_b32_e32 v95, v95, v141
	ds_write_b16 v95, v94 offset:16384
	v_sub_f32_e32 v95, v93, v154
	v_mul_f32_e32 v95, 0x3fb8aa3b, v95
	v_exp_f32_e32 v95, v95
	s_nop 0
	v_mul_f32_e32 v95, v97, v95
	s_nop 0
	v_mul_f32_e32 v95, v156, v95
	v_cvt_pk_bf16_f32 v95, v95, s0
	v_cmp_ne_u32_e32 vcc, 0, v211
	v_ashrrev_i32_e32 v119, 31, v118
	s_nop 0
	v_cndmask_b32_e32 v94, 0, v95, vcc
	v_bitop3_b32 v95, v118, v113, 7 bitop3:0x6c
	v_lshl_add_u32 v95, v95, 4, v161
	v_or_b32_e32 v95, v95, v141
	ds_write_b16 v95, v94 offset:16384
	v_add_u32_e32 v94, 48, v110
	v_lshrrev_b32_e32 v95, 3, v94
	v_bitop3_b32 v90, v142, v95, 4 bitop3:0x6c
	v_lshl_add_u32 v90, v90, 4, v158
	v_or_b32_e32 v90, v90, v141
	v_cmp_ne_u32_e32 vcc, 0, v212
	v_ashrrev_i32_e32 v113, 31, v112
	s_nop 0
	v_cndmask_b32_e32 v86, 0, v86, vcc
	ds_write_b16 v90, v86 offset:16384
	v_sub_f32_e32 v90, v91, v155
	v_mul_f32_e32 v90, 0x3fb8aa3b, v90
	v_exp_f32_e32 v90, v90
	s_nop 0
	v_mul_f32_e32 v87, v87, v90
	s_nop 0
	v_mul_f32_e32 v87, v157, v87
	v_cvt_pk_bf16_f32 v87, v87, s0
	v_cmp_ne_u32_e32 vcc, 0, v213
	s_nop 1
	s_nop 0
	v_cndmask_b32_e32 v86, 0, v87, vcc
	v_bitop3_b32 v87, v114, v95, 5 bitop3:0x6c
	v_lshl_add_u32 v87, v87, 4, v159
	v_or_b32_e32 v87, v87, v141
	ds_write_b16 v87, v86 offset:16384
	v_sub_f32_e32 v87, v92, v155
	v_mul_f32_e32 v87, 0x3fb8aa3b, v87
	v_exp_f32_e32 v87, v87
	s_nop 0
	v_mul_f32_e32 v87, v88, v87
	s_nop 0
	v_mul_f32_e32 v87, v157, v87
	v_cvt_pk_bf16_f32 v87, v87, s0
	v_cmp_ne_u32_e32 vcc, 0, v214
	s_nop 1
	s_nop 0
	v_cndmask_b32_e32 v86, 0, v87, vcc
	v_bitop3_b32 v87, v116, v95, 6 bitop3:0x6c
	v_lshl_add_u32 v87, v87, 4, v160
	v_or_b32_e32 v87, v87, v141
	ds_write_b16 v87, v86 offset:16384
	v_sub_f32_e32 v87, v93, v155
	v_mul_f32_e32 v87, 0x3fb8aa3b, v87
	v_exp_f32_e32 v87, v87
	s_nop 0
	v_mul_f32_e32 v87, v89, v87
	s_nop 0
	v_mul_f32_e32 v87, v157, v87
	v_cvt_pk_bf16_f32 v87, v87, s0
	v_cmp_ne_u32_e32 vcc, 0, v215
	v_lshlrev_b32_e32 v88, 4, v111
	v_ashrrev_i32_e32 v111, 31, v110
	v_cndmask_b32_e32 v86, 0, v87, vcc
	v_bitop3_b32 v87, v118, v95, 7 bitop3:0x6c
	v_lshl_add_u32 v87, v87, 4, v161
	v_or_b32_e32 v87, v87, v141
	ds_write_b16 v87, v86 offset:16384
	v_lshlrev_b32_e32 v86, 7, v110
	v_add_u32_e32 v89, v137, v86
	s_waitcnt lgkmcnt(0)
	s_barrier
	v_add_u32_e32 v87, v89, v88
	ds_read_b128 v[90:93], v87 offset:16384
	v_add_u32_e32 v87, v86, v88
	ds_read_b128 v[94:97], v87 offset:49152
	ds_read_b128 v[154:157], v87 offset:51200
	v_lshlrev_b32_e32 v87, 4, v148
	v_add_u32_e32 v89, v89, v87
	ds_read_b128 v[158:161], v89 offset:16384
	v_add_u32_e32 v89, v86, v87
	s_waitcnt lgkmcnt(2)
	v_mfma_f32_16x16x32_bf16 v[94:97], v[90:93], v[94:97], 0
	s_waitcnt lgkmcnt(1)
	v_mfma_f32_16x16x32_bf16 v[90:93], v[90:93], v[154:157], 0
	ds_read_b128 v[154:157], v89 offset:49152
	ds_read_b128 v[162:165], v89 offset:51200
	v_add_u32_e32 v89, v138, v117
	v_ashrrev_i32_e32 v117, 31, v116
	s_waitcnt lgkmcnt(1)
	v_mfma_f32_16x16x32_bf16 v[94:97], v[158:161], v[154:157], v[94:97]
	s_waitcnt lgkmcnt(0)
	v_mfma_f32_16x16x32_bf16 v[90:93], v[158:161], v[162:165], v[90:93]
	ds_read_b128 v[154:157], v149 offset:57344
	ds_read_b128 v[158:161], v149 offset:61440
	s_waitcnt lgkmcnt(1)
	v_mfma_f32_16x16x32_bf16 v[154:157], v[70:73], v[154:157], 0
	s_waitcnt lgkmcnt(0)
	v_mfma_f32_16x16x32_bf16 v[70:73], v[70:73], v[158:161], 0
	ds_read_b128 v[158:161], v174 offset:57344
	ds_read_b128 v[162:165], v174 offset:61440
	s_waitcnt lgkmcnt(1)
	v_mfma_f32_16x16x32_bf16 v[154:157], v[74:77], v[158:161], v[154:157]
	s_waitcnt lgkmcnt(0)
	v_mfma_f32_16x16x32_bf16 v[70:73], v[74:77], v[162:165], v[70:73]
	ds_read_b128 v[74:77], v175 offset:57344
	ds_read_b128 v[158:161], v175 offset:61440
	s_waitcnt lgkmcnt(1)
	v_mfma_f32_16x16x32_bf16 v[74:77], v[78:81], v[74:77], v[154:157]
	s_nop 2
	ds_read_b128 v[154:157], v176 offset:57344
	s_waitcnt lgkmcnt(1)
	v_mfma_f32_16x16x32_bf16 v[70:73], v[78:81], v[158:161], v[70:73]
	ds_read_b128 v[78:81], v176 offset:61440
	s_waitcnt lgkmcnt(1)
	v_mfma_f32_16x16x32_bf16 v[74:77], v[82:85], v[154:157], v[74:77]
	ds_read_b128 v[154:157], v89
	s_waitcnt lgkmcnt(1)
	v_mfma_f32_16x16x32_bf16 v[70:73], v[82:85], v[78:81], v[70:73]
	v_lshl_add_u64 v[80:81], s[52:53], 0, v[112:113]
	v_lshl_add_u64 v[78:79], v[110:111], 1, s[50:51]
	s_waitcnt lgkmcnt(0)
	s_nop 1
	v_fma_f32 v74, v74, v154, v94
	v_lshlrev_b64 v[80:81], 11, v[80:81]
	v_cvt_pk_bf16_f32 v74, v74, s0
	v_lshl_add_u64 v[80:81], v[78:79], 0, v[80:81]
	global_store_short v[80:81], v74, off
	v_fma_f32 v74, v75, v155, v95
	v_cvt_pk_bf16_f32 v82, v74, s0
	v_lshl_add_u64 v[74:75], s[52:53], 0, v[114:115]
	v_lshlrev_b64 v[74:75], 11, v[74:75]
	v_lshl_add_u64 v[74:75], v[78:79], 0, v[74:75]
	v_fma_f32 v70, v154, v70, v90
	global_store_short v[74:75], v82, off
	v_lshl_add_u64 v[82:83], s[52:53], 0, v[116:117]
	v_cvt_pk_bf16_f32 v70, v70, s0
	v_fma_f32 v76, v76, v156, v96
	v_lshlrev_b64 v[82:83], 11, v[82:83]
	global_store_short v[80:81], v70, off offset:32
	v_fma_f32 v70, v71, v155, v91
	v_cvt_pk_bf16_f32 v76, v76, s0
	v_lshl_add_u64 v[82:83], v[78:79], 0, v[82:83]
	v_cvt_pk_bf16_f32 v70, v70, s0
	global_store_short v[82:83], v76, off
	v_fmac_f32_e32 v97, v77, v157
	v_lshl_add_u64 v[76:77], s[52:53], 0, v[118:119]
	global_store_short v[74:75], v70, off offset:32
	v_fma_f32 v70, v72, v156, v92
	v_lshlrev_b64 v[76:77], 11, v[76:77]
	v_cvt_pk_bf16_f32 v70, v70, s0
	v_fmac_f32_e32 v93, v73, v157
	v_cvt_pk_bf16_f32 v84, v97, s0
	v_lshl_add_u64 v[76:77], v[78:79], 0, v[76:77]
	global_store_short v[82:83], v70, off offset:32
	v_cvt_pk_bf16_f32 v70, v93, s0
	global_store_short v[76:77], v84, off
	global_store_short v[76:77], v70, off offset:32
